# agg1: degree-rank group of each wave chosen from its SIMD id and the block's ordinal on the CU (balanced per-SIMD stage load, falls back to wave id if SIMDs not distinct); barrier moved before the ran
# speedup vs baseline: 1.0089x; 1.0089x over previous
_Z11agg1_kernelPKDF16_PKfS2_PKiS4_S2_S2_PDF16_PfS6_i:
	s_load_dwordx8 s[4:11], s[0:1], 0x0
	s_load_dwordx8 s[12:19], s[0:1], 0x20
	s_load_dwordx4 s[20:23], s[0:1], 0x40
	s_load_dword s24, s[0:1], 0x50
	v_lshlrev_b32_e32 v32, 2, v0
	v_readfirstlane_b32 s25, v0
	s_lshl_b32 s26, s2, 5
	v_and_b32_e32 v64, 7, v0
	v_bfe_u32 v65, v0, 3, 3
	v_and_b32_e32 v45, 31, v0
	s_lshr_b32 s25, s25, 6
	s_getreg_b32 s30, hwreg(HW_REG_HW_ID, 4, 2)
	s_lshr_b32 s31, s2, 8
	s_lshl_b32 s31, s31, 3
	s_mov_b32 s44, 0x276c9c8d
	s_mov_b32 s45, 0xe46393
	s_and_b32 s47, s2, 0xff
	s_cmp_lt_u32 s47, 27
	s_cselect_b32 s44, 0xb1784b63, s44
	s_cselect_b32 s45, 0x1e4ee4, s45
	s_lshr_b64 s[44:45], s[44:45], s31
	s_lshl_b32 s31, s30, 1
	s_lshr_b32 s44, s44, s31
	s_and_b32 s44, s44, 3
	s_lshl_b32 s45, 1, s30
	s_lshl_b32 s46, s25, 2
	s_addk_i32 s46, 0x2800
	v_mov_b32_e32 v49, s45
	v_mov_b32_e32 v50, s46
	ds_write_b32 v50, v49
	v_lshlrev_b32_e32 v1, 1, v64
	v_add_u32_e32 v46, s26, v45
	s_waitcnt lgkmcnt(0)
	global_load_dword v33, v32, s[14:15]
	global_load_dword v34, v32, s[16:17]
	s_add_i32 s28, s24, -1
	v_cmp_gt_i32_e64 s[38:39], s24, v46
	v_min_i32_e32 v46, s28, v46
	v_lshlrev_b32_e32 v47, 2, v46
	global_load_dword v44, v47, s[10:11]
	global_load_dword v48, v47, s[10:11] offset:4
	s_lshl_b32 s27, s25, 11
	v_lshlrev_b32_e32 v62, 6, v64
	v_add_u32_e32 v62, 0x2000, v62
	v_cmp_eq_u32_e64 s[34:35], 0, v64
	v_lshlrev_b32_e32 v35, 8, v64
	v_lshl_add_u32 v35, v65, 4, v35
	v_add_u32_e32 v63, s27, v35
	v_mov_b32_e32 v36, 0
	v_mov_b32_e32 v37, 0
	v_mov_b32_e32 v38, 0
	v_mov_b32_e32 v39, 0
	s_waitcnt vmcnt(2)
	ds_write2st64_b32 v32, v33, v34 offset0:32 offset1:36
	ds_write_b128 v63, v[36:39]
	ds_write_b128 v63, v[36:39] offset:128
	s_waitcnt vmcnt(0)
	v_sub_u32_e32 v48, v48, v44
	v_add_u32_e32 v48, 1, v48
	v_cndmask_b32_e64 v48, 0, v48, s[38:39]
	v_lshl_or_b32 v40, v48, 5, v45
	s_nop 1
	v_mov_b32_dpp v41, v40 quad_perm:[1,0,3,2] row_mask:0xf bank_mask:0xf
	s_mov_b32 s40, 0x99999999
	s_mov_b32 s41, 0x99999999
	v_min_u32_e32 v42, v40, v41
	v_max_u32_e32 v43, v40, v41
	v_cndmask_b32_e64 v40, v42, v43, s[40:41]
	s_nop 1
	v_mov_b32_dpp v41, v40 quad_perm:[2,3,0,1] row_mask:0xf bank_mask:0xf
	s_mov_b32 s40, 0xc3c3c3c3
	s_mov_b32 s41, 0xc3c3c3c3
	v_min_u32_e32 v42, v40, v41
	v_max_u32_e32 v43, v40, v41
	v_cndmask_b32_e64 v40, v42, v43, s[40:41]
	s_nop 1
	v_mov_b32_dpp v41, v40 quad_perm:[1,0,3,2] row_mask:0xf bank_mask:0xf
	s_mov_b32 s40, 0xa5a5a5a5
	s_mov_b32 s41, 0xa5a5a5a5
	v_min_u32_e32 v42, v40, v41
	v_max_u32_e32 v43, v40, v41
	v_cndmask_b32_e64 v40, v42, v43, s[40:41]
	s_nop 1
	v_mov_b32_dpp v41, v40 row_shl:4 row_mask:0xf bank_mask:0x5
	v_mov_b32_dpp v41, v40 row_shr:4 row_mask:0xf bank_mask:0xa
	s_mov_b32 s40, 0xf00ff00f
	s_mov_b32 s41, 0xf00ff00f
	v_min_u32_e32 v42, v40, v41
	v_max_u32_e32 v43, v40, v41
	v_cndmask_b32_e64 v40, v42, v43, s[40:41]
	s_nop 1
	v_mov_b32_dpp v41, v40 quad_perm:[2,3,0,1] row_mask:0xf bank_mask:0xf
	s_mov_b32 s40, 0xcc33cc33
	s_mov_b32 s41, 0xcc33cc33
	v_min_u32_e32 v42, v40, v41
	v_max_u32_e32 v43, v40, v41
	v_cndmask_b32_e64 v40, v42, v43, s[40:41]
	s_nop 1
	v_mov_b32_dpp v41, v40 quad_perm:[1,0,3,2] row_mask:0xf bank_mask:0xf
	s_mov_b32 s40, 0xaa55aa55
	s_mov_b32 s41, 0xaa55aa55
	v_min_u32_e32 v42, v40, v41
	v_max_u32_e32 v43, v40, v41
	v_cndmask_b32_e64 v40, v42, v43, s[40:41]
	s_nop 1
	v_mov_b32_dpp v41, v40 row_ror:8 row_mask:0xf bank_mask:0xf
	s_mov_b32 s40, 0xff0000ff
	s_mov_b32 s41, 0xff0000ff
	v_min_u32_e32 v42, v40, v41
	v_max_u32_e32 v43, v40, v41
	v_cndmask_b32_e64 v40, v42, v43, s[40:41]
	s_nop 1
	v_mov_b32_dpp v41, v40 row_shl:4 row_mask:0xf bank_mask:0x5
	v_mov_b32_dpp v41, v40 row_shr:4 row_mask:0xf bank_mask:0xa
	s_mov_b32 s40, 0xf0f00f0f
	s_mov_b32 s41, 0xf0f00f0f
	v_min_u32_e32 v42, v40, v41
	v_max_u32_e32 v43, v40, v41
	v_cndmask_b32_e64 v40, v42, v43, s[40:41]
	s_nop 1
	v_mov_b32_dpp v41, v40 quad_perm:[2,3,0,1] row_mask:0xf bank_mask:0xf
	s_mov_b32 s40, 0xcccc3333
	s_mov_b32 s41, 0xcccc3333
	v_min_u32_e32 v42, v40, v41
	v_max_u32_e32 v43, v40, v41
	v_cndmask_b32_e64 v40, v42, v43, s[40:41]
	s_nop 1
	v_mov_b32_dpp v41, v40 quad_perm:[1,0,3,2] row_mask:0xf bank_mask:0xf
	s_mov_b32 s40, 0xaaaa5555
	s_mov_b32 s41, 0xaaaa5555
	v_min_u32_e32 v42, v40, v41
	v_max_u32_e32 v43, v40, v41
	v_cndmask_b32_e64 v40, v42, v43, s[40:41]
	ds_swizzle_b32 v41, v40 offset:swizzle(SWAP,16)
	s_waitcnt lgkmcnt(0)
	s_mov_b32 s40, 0xffff
	s_mov_b32 s41, 0xffff
	v_min_u32_e32 v42, v40, v41
	v_max_u32_e32 v43, v40, v41
	v_cndmask_b32_e64 v40, v42, v43, s[40:41]
	s_nop 1
	v_mov_b32_dpp v41, v40 row_ror:8 row_mask:0xf bank_mask:0xf
	s_mov_b32 s40, 0xff00ff
	s_mov_b32 s41, 0xff00ff
	v_min_u32_e32 v42, v40, v41
	v_max_u32_e32 v43, v40, v41
	v_cndmask_b32_e64 v40, v42, v43, s[40:41]
	s_nop 1
	v_mov_b32_dpp v41, v40 row_shl:4 row_mask:0xf bank_mask:0x5
	v_mov_b32_dpp v41, v40 row_shr:4 row_mask:0xf bank_mask:0xa
	s_mov_b32 s40, 0xf0f0f0f
	s_mov_b32 s41, 0xf0f0f0f
	v_min_u32_e32 v42, v40, v41
	v_max_u32_e32 v43, v40, v41
	v_cndmask_b32_e64 v40, v42, v43, s[40:41]
	s_nop 1
	v_mov_b32_dpp v41, v40 quad_perm:[2,3,0,1] row_mask:0xf bank_mask:0xf
	s_mov_b32 s40, 0x33333333
	s_mov_b32 s41, 0x33333333
	v_min_u32_e32 v42, v40, v41
	v_max_u32_e32 v43, v40, v41
	v_cndmask_b32_e64 v40, v42, v43, s[40:41]
	s_nop 1
	v_mov_b32_dpp v41, v40 quad_perm:[1,0,3,2] row_mask:0xf bank_mask:0xf
	s_mov_b32 s40, 0x55555555
	s_mov_b32 s41, 0x55555555
	v_min_u32_e32 v42, v40, v41
	v_max_u32_e32 v43, v40, v41
	v_cndmask_b32_e64 v40, v42, v43, s[40:41]
	v_mov_b32_e32 v50, 0x2800
	s_waitcnt lgkmcnt(0)
	s_barrier
	ds_read_b128 v[52:55], v50
	s_waitcnt lgkmcnt(0)
	v_or3_b32 v52, v52, v53, v54
	v_or_b32_e32 v52, v52, v55
	s_nop 0
	v_readfirstlane_b32 s46, v52
	s_cmp_eq_u32 s46, 15
	s_cselect_b32 s44, s44, s25
	s_lshl_b32 s40, s44, 3
	v_add_u32_e32 v45, s40, v65
	v_lshlrev_b32_e32 v45, 2, v45
	ds_bpermute_b32 v46, v45, v40
	s_waitcnt lgkmcnt(0)
	v_and_b32_e32 v15, 31, v46
	v_lshrrev_b32_e32 v11, 5, v46
	v_lshlrev_b32_e32 v47, 2, v15
	ds_bpermute_b32 v10, v47, v44
	v_add_u32_e32 v66, s26, v15
	v_min_i32_e32 v66, s28, v66
	v_cmp_lt_u32_e64 s[36:37], 0, v11
	v_lshlrev_b32_e32 v4, 2, v66
	v_lshlrev_b32_e32 v35, 2, v64
	v_lshl_or_b32 v35, v66, 5, v35
	global_load_dword v9, v35, s[8:9]
	v_lshrrev_b32_e32 v3, 3, v15
	v_lshlrev_b32_e32 v3, 11, v3
	v_and_b32_e32 v47, 7, v15
	v_lshl_add_u32 v3, v47, 1, v3
	v_lshl_add_u32 v3, v64, 4, v3
	v_readfirstlane_b32 s29, v11
	s_waitcnt lgkmcnt(0)
	v_add_u32_e32 v67, v10, v64
	v_lshlrev_b32_e32 v67, 2, v67
	v_mov_b32_e32 v5, s24
	v_mov_b32_e32 v6, s24
	v_mov_b32_e32 v7, s24
	v_mov_b32_e32 v8, s24
	v_mov_b32_e32 v69, s24
	v_cndmask_b32_e64 v5, v5, v66, s[34:35]
	v_cmp_gt_i32_e32 vcc, v11, v64
	s_andn2_b64 s[40:41], vcc, s[34:35]
	s_and_saveexec_b64 s[32:33], s[40:41]
	global_load_dword v5, v67, s[12:13] offset:-4
	s_mov_b64 exec, s[32:33]
	v_add_u32_e32 v68, 8, v64
	v_cmp_gt_i32_e32 vcc, v11, v68
	s_and_saveexec_b64 s[32:33], vcc
	global_load_dword v6, v67, s[12:13] offset:28
	s_mov_b64 exec, s[32:33]
	v_add_u32_e32 v68, 16, v64
	v_cmp_gt_i32_e32 vcc, v11, v68
	s_and_saveexec_b64 s[32:33], vcc
	global_load_dword v7, v67, s[12:13] offset:60
	s_mov_b64 exec, s[32:33]
	v_add_u32_e32 v68, 24, v64
	v_cmp_gt_i32_e32 vcc, v11, v68
	s_and_saveexec_b64 s[32:33], vcc
	global_load_dword v8, v67, s[12:13] offset:92
	s_mov_b64 exec, s[32:33]
	v_add_u32_e32 v68, 32, v64
	v_cmp_gt_i32_e32 vcc, v11, v68
	s_and_saveexec_b64 s[32:33], vcc
	global_load_dword v69, v67, s[12:13] offset:124
	s_mov_b64 exec, s[32:33]
	s_waitcnt vmcnt(0)
	v_lshlrev_b32_e32 v5, 4, v5
	v_lshlrev_b32_e32 v6, 4, v6
	v_lshlrev_b32_e32 v7, 4, v7
	v_lshlrev_b32_e32 v8, 4, v8
	v_lshlrev_b32_e32 v69, 4, v69
	s_mov_b32 s42, 0
	s_mov_b32 s43, 0
	ds_swizzle_b32 v32, v5 offset:swizzle(BITMASK_PERM, "pp000")
	ds_swizzle_b32 v33, v5 offset:swizzle(BITMASK_PERM, "pp001")
	ds_swizzle_b32 v34, v5 offset:swizzle(BITMASK_PERM, "pp010")
	ds_swizzle_b32 v35, v5 offset:swizzle(BITMASK_PERM, "pp011")
	s_cmp_lt_i32 s29, 3
	s_cbranch_scc1 .Lagg_first_half
	s_waitcnt lgkmcnt(0)
	v_or_b32_e32 v32, v32, v1
	v_or_b32_e32 v33, v33, v1
	v_or_b32_e32 v34, v34, v1
	v_or_b32_e32 v35, v35, v1
	global_load_ushort v36, v32, s[6:7]
	global_load_ushort v37, v33, s[6:7]
	global_load_ushort v38, v34, s[6:7]
	global_load_ushort v39, v35, s[6:7]
	v_lshlrev_b32_e32 v32, 3, v32
	v_lshlrev_b32_e32 v33, 3, v33
	v_lshlrev_b32_e32 v34, 3, v34
	v_lshlrev_b32_e32 v35, 3, v35
	global_load_dwordx4 v[40:43], v32, s[4:5]
	global_load_dwordx4 v[44:47], v33, s[4:5]
	global_load_dwordx4 v[48:51], v34, s[4:5]
	global_load_dwordx4 v[52:55], v35, s[4:5]
	ds_swizzle_b32 v32, v5 offset:swizzle(BITMASK_PERM, "pp100")
	ds_swizzle_b32 v33, v5 offset:swizzle(BITMASK_PERM, "pp101")
	ds_swizzle_b32 v34, v5 offset:swizzle(BITMASK_PERM, "pp110")
	ds_swizzle_b32 v35, v5 offset:swizzle(BITMASK_PERM, "pp111")
	s_waitcnt vmcnt(4)
	v_fma_mix_f32 v36, v36, 1.0, v9 op_sel_hi:[1,0,0]
	v_fma_mix_f32 v37, v37, 1.0, v9 op_sel_hi:[1,0,0]
	v_fma_mix_f32 v38, v38, 1.0, v9 op_sel_hi:[1,0,0]
	v_fma_mix_f32 v39, v39, 1.0, v9 op_sel_hi:[1,0,0]
	v_mul_f32_e32 v58, 0x3e4ccccd, v36
	v_mul_f32_e32 v59, 0x3e4ccccd, v37
	v_mul_f32_e32 v60, 0x3e4ccccd, v38
	v_mul_f32_e32 v61, 0x3e4ccccd, v39
	v_max_f32_e32 v36, v36, v58
	v_max_f32_e32 v37, v37, v59
	v_max_f32_e32 v38, v38, v60
	v_max_f32_e32 v39, v39, v61
	v_max3_f32 v56, v36, v37, v38
	v_max_f32_e32 v13, v56, v39
	v_sub_f32_e32 v36, v36, v13
	v_sub_f32_e32 v37, v37, v13
	v_sub_f32_e32 v38, v38, v13
	v_sub_f32_e32 v39, v39, v13
	v_exp_f32_e32 v36, v36
	v_exp_f32_e32 v37, v37
	v_exp_f32_e32 v38, v38
	v_exp_f32_e32 v39, v39
	s_nop 0
	v_add_f32_e32 v14, v36, v37
	v_add_f32_e32 v14, v14, v38
	v_add_f32_e32 v14, v14, v39
	s_waitcnt vmcnt(3)
	v_cvt_scalef32_pk_f16_fp8 v58, v40, 1.0
	v_cvt_scalef32_pk_f16_fp8 v59, v40, 1.0 op_sel:[1,0,0]
	v_cvt_scalef32_pk_f16_fp8 v60, v41, 1.0
	v_cvt_scalef32_pk_f16_fp8 v61, v41, 1.0 op_sel:[1,0,0]
	v_fma_mix_f32 v16, v58, v36, 0 op_sel_hi:[1,0,0]
	v_fma_mix_f32 v17, v58, v36, 0 op_sel:[1,0,0] op_sel_hi:[1,0,0]
	v_fma_mix_f32 v18, v59, v36, 0 op_sel_hi:[1,0,0]
	v_fma_mix_f32 v19, v59, v36, 0 op_sel:[1,0,0] op_sel_hi:[1,0,0]
	v_fma_mix_f32 v20, v60, v36, 0 op_sel_hi:[1,0,0]
	v_fma_mix_f32 v21, v60, v36, 0 op_sel:[1,0,0] op_sel_hi:[1,0,0]
	v_fma_mix_f32 v22, v61, v36, 0 op_sel_hi:[1,0,0]
	v_fma_mix_f32 v23, v61, v36, 0 op_sel:[1,0,0] op_sel_hi:[1,0,0]
	v_cvt_scalef32_pk_f16_fp8 v58, v42, 1.0
	v_cvt_scalef32_pk_f16_fp8 v59, v42, 1.0 op_sel:[1,0,0]
	v_cvt_scalef32_pk_f16_fp8 v60, v43, 1.0
	v_cvt_scalef32_pk_f16_fp8 v61, v43, 1.0 op_sel:[1,0,0]
	v_fma_mix_f32 v24, v58, v36, 0 op_sel_hi:[1,0,0]
	v_fma_mix_f32 v25, v58, v36, 0 op_sel:[1,0,0] op_sel_hi:[1,0,0]
	v_fma_mix_f32 v26, v59, v36, 0 op_sel_hi:[1,0,0]
	v_fma_mix_f32 v27, v59, v36, 0 op_sel:[1,0,0] op_sel_hi:[1,0,0]
	v_fma_mix_f32 v28, v60, v36, 0 op_sel_hi:[1,0,0]
	v_fma_mix_f32 v29, v60, v36, 0 op_sel:[1,0,0] op_sel_hi:[1,0,0]
	v_fma_mix_f32 v30, v61, v36, 0 op_sel_hi:[1,0,0]
	v_fma_mix_f32 v31, v61, v36, 0 op_sel:[1,0,0] op_sel_hi:[1,0,0]
	s_waitcnt vmcnt(2)
	v_cvt_scalef32_pk_f16_fp8 v58, v44, 1.0
	v_cvt_scalef32_pk_f16_fp8 v59, v44, 1.0 op_sel:[1,0,0]
	v_cvt_scalef32_pk_f16_fp8 v60, v45, 1.0
	v_cvt_scalef32_pk_f16_fp8 v61, v45, 1.0 op_sel:[1,0,0]
	v_fma_mix_f32 v16, v58, v37, v16 op_sel_hi:[1,0,0]
	v_fma_mix_f32 v17, v58, v37, v17 op_sel:[1,0,0] op_sel_hi:[1,0,0]
	v_fma_mix_f32 v18, v59, v37, v18 op_sel_hi:[1,0,0]
	v_fma_mix_f32 v19, v59, v37, v19 op_sel:[1,0,0] op_sel_hi:[1,0,0]
	v_fma_mix_f32 v20, v60, v37, v20 op_sel_hi:[1,0,0]
	v_fma_mix_f32 v21, v60, v37, v21 op_sel:[1,0,0] op_sel_hi:[1,0,0]
	v_fma_mix_f32 v22, v61, v37, v22 op_sel_hi:[1,0,0]
	v_fma_mix_f32 v23, v61, v37, v23 op_sel:[1,0,0] op_sel_hi:[1,0,0]
	v_cvt_scalef32_pk_f16_fp8 v58, v46, 1.0
	v_cvt_scalef32_pk_f16_fp8 v59, v46, 1.0 op_sel:[1,0,0]
	v_cvt_scalef32_pk_f16_fp8 v60, v47, 1.0
	v_cvt_scalef32_pk_f16_fp8 v61, v47, 1.0 op_sel:[1,0,0]
	v_fma_mix_f32 v24, v58, v37, v24 op_sel_hi:[1,0,0]
	v_fma_mix_f32 v25, v58, v37, v25 op_sel:[1,0,0] op_sel_hi:[1,0,0]
	v_fma_mix_f32 v26, v59, v37, v26 op_sel_hi:[1,0,0]
	v_fma_mix_f32 v27, v59, v37, v27 op_sel:[1,0,0] op_sel_hi:[1,0,0]
	v_fma_mix_f32 v28, v60, v37, v28 op_sel_hi:[1,0,0]
	v_fma_mix_f32 v29, v60, v37, v29 op_sel:[1,0,0] op_sel_hi:[1,0,0]
	v_fma_mix_f32 v30, v61, v37, v30 op_sel_hi:[1,0,0]
	v_fma_mix_f32 v31, v61, v37, v31 op_sel:[1,0,0] op_sel_hi:[1,0,0]
	s_waitcnt vmcnt(1)
	v_cvt_scalef32_pk_f16_fp8 v58, v48, 1.0
	v_cvt_scalef32_pk_f16_fp8 v59, v48, 1.0 op_sel:[1,0,0]
	v_cvt_scalef32_pk_f16_fp8 v60, v49, 1.0
	v_cvt_scalef32_pk_f16_fp8 v61, v49, 1.0 op_sel:[1,0,0]
	v_fma_mix_f32 v16, v58, v38, v16 op_sel_hi:[1,0,0]
	v_fma_mix_f32 v17, v58, v38, v17 op_sel:[1,0,0] op_sel_hi:[1,0,0]
	v_fma_mix_f32 v18, v59, v38, v18 op_sel_hi:[1,0,0]
	v_fma_mix_f32 v19, v59, v38, v19 op_sel:[1,0,0] op_sel_hi:[1,0,0]
	v_fma_mix_f32 v20, v60, v38, v20 op_sel_hi:[1,0,0]
	v_fma_mix_f32 v21, v60, v38, v21 op_sel:[1,0,0] op_sel_hi:[1,0,0]
	v_fma_mix_f32 v22, v61, v38, v22 op_sel_hi:[1,0,0]
	v_fma_mix_f32 v23, v61, v38, v23 op_sel:[1,0,0] op_sel_hi:[1,0,0]
	v_cvt_scalef32_pk_f16_fp8 v58, v50, 1.0
	v_cvt_scalef32_pk_f16_fp8 v59, v50, 1.0 op_sel:[1,0,0]
	v_cvt_scalef32_pk_f16_fp8 v60, v51, 1.0
	v_cvt_scalef32_pk_f16_fp8 v61, v51, 1.0 op_sel:[1,0,0]
	v_fma_mix_f32 v24, v58, v38, v24 op_sel_hi:[1,0,0]
	v_fma_mix_f32 v25, v58, v38, v25 op_sel:[1,0,0] op_sel_hi:[1,0,0]
	v_fma_mix_f32 v26, v59, v38, v26 op_sel_hi:[1,0,0]
	v_fma_mix_f32 v27, v59, v38, v27 op_sel:[1,0,0] op_sel_hi:[1,0,0]
	v_fma_mix_f32 v28, v60, v38, v28 op_sel_hi:[1,0,0]
	v_fma_mix_f32 v29, v60, v38, v29 op_sel:[1,0,0] op_sel_hi:[1,0,0]
	v_fma_mix_f32 v30, v61, v38, v30 op_sel_hi:[1,0,0]
	v_fma_mix_f32 v31, v61, v38, v31 op_sel:[1,0,0] op_sel_hi:[1,0,0]
	s_waitcnt vmcnt(0)
	v_cvt_scalef32_pk_f16_fp8 v58, v52, 1.0
	v_cvt_scalef32_pk_f16_fp8 v59, v52, 1.0 op_sel:[1,0,0]
	v_cvt_scalef32_pk_f16_fp8 v60, v53, 1.0
	v_cvt_scalef32_pk_f16_fp8 v61, v53, 1.0 op_sel:[1,0,0]
	v_fma_mix_f32 v16, v58, v39, v16 op_sel_hi:[1,0,0]
	v_fma_mix_f32 v17, v58, v39, v17 op_sel:[1,0,0] op_sel_hi:[1,0,0]
	v_fma_mix_f32 v18, v59, v39, v18 op_sel_hi:[1,0,0]
	v_fma_mix_f32 v19, v59, v39, v19 op_sel:[1,0,0] op_sel_hi:[1,0,0]
	v_fma_mix_f32 v20, v60, v39, v20 op_sel_hi:[1,0,0]
	v_fma_mix_f32 v21, v60, v39, v21 op_sel:[1,0,0] op_sel_hi:[1,0,0]
	v_fma_mix_f32 v22, v61, v39, v22 op_sel_hi:[1,0,0]
	v_fma_mix_f32 v23, v61, v39, v23 op_sel:[1,0,0] op_sel_hi:[1,0,0]
	v_cvt_scalef32_pk_f16_fp8 v58, v54, 1.0
	v_cvt_scalef32_pk_f16_fp8 v59, v54, 1.0 op_sel:[1,0,0]
	v_cvt_scalef32_pk_f16_fp8 v60, v55, 1.0
	v_cvt_scalef32_pk_f16_fp8 v61, v55, 1.0 op_sel:[1,0,0]
	v_fma_mix_f32 v24, v58, v39, v24 op_sel_hi:[1,0,0]
	v_fma_mix_f32 v25, v58, v39, v25 op_sel:[1,0,0] op_sel_hi:[1,0,0]
	v_fma_mix_f32 v26, v59, v39, v26 op_sel_hi:[1,0,0]
	v_fma_mix_f32 v27, v59, v39, v27 op_sel:[1,0,0] op_sel_hi:[1,0,0]
	v_fma_mix_f32 v28, v60, v39, v28 op_sel_hi:[1,0,0]
	v_fma_mix_f32 v29, v60, v39, v29 op_sel:[1,0,0] op_sel_hi:[1,0,0]
	v_fma_mix_f32 v30, v61, v39, v30 op_sel_hi:[1,0,0]
	v_fma_mix_f32 v31, v61, v39, v31 op_sel:[1,0,0] op_sel_hi:[1,0,0]
	s_sub_i32 s29, s29, 4
	s_branch .Lagg_B

	.amdhsa_kernel _Z11agg1_kernelPKDF16_PKfS2_PKiS4_S2_S2_PDF16_PfS6_i
		.amdhsa_group_segment_fixed_size 10256
		.amdhsa_private_segment_fixed_size 0
		.amdhsa_kernarg_size 84
		.amdhsa_user_sgpr_count 2
		.amdhsa_user_sgpr_dispatch_ptr 0
		.amdhsa_user_sgpr_queue_ptr 0
		.amdhsa_user_sgpr_kernarg_segment_ptr 1
		.amdhsa_user_sgpr_dispatch_id 0
		.amdhsa_user_sgpr_kernarg_preload_length 0
		.amdhsa_user_sgpr_kernarg_preload_offset 0
		.amdhsa_user_sgpr_private_segment_size 0
		.amdhsa_uses_dynamic_stack 0
		.amdhsa_enable_private_segment 0
		.amdhsa_system_sgpr_workgroup_id_x 1
		.amdhsa_system_sgpr_workgroup_id_y 0
		.amdhsa_system_sgpr_workgroup_id_z 0
		.amdhsa_system_sgpr_workgroup_info 0
		.amdhsa_system_vgpr_workitem_id 0
		.amdhsa_next_free_vgpr 70
		.amdhsa_next_free_sgpr 48
		.amdhsa_accum_offset 72
		.amdhsa_reserve_vcc 1
		.amdhsa_float_round_mode_32 0
		.amdhsa_float_round_mode_16_64 0
		.amdhsa_float_denorm_mode_32 3
		.amdhsa_float_denorm_mode_16_64 3
		.amdhsa_dx10_clamp 1
		.amdhsa_ieee_mode 1
		.amdhsa_fp16_overflow 0
		.amdhsa_tg_split 0
		.amdhsa_exception_fp_ieee_invalid_op 0
		.amdhsa_exception_fp_denorm_src 0
		.amdhsa_exception_fp_ieee_div_zero 0
		.amdhsa_exception_fp_ieee_overflow 0
		.amdhsa_exception_fp_ieee_underflow 0
		.amdhsa_exception_fp_ieee_inexact 0
		.amdhsa_exception_int_div_zero 0
	.end_amdhsa_kernel

amdhsa.kernels:
  - .agpr_count:     0
    .args:
      - .actual_access:  read_only
        .address_space:  global
        .offset:         0
        .size:           8
        .value_kind:     global_buffer
      - .actual_access:  read_only
        .address_space:  global
        .offset:         8
        .size:           8
        .value_kind:     global_buffer
      - .actual_access:  read_only
        .address_space:  global
        .offset:         16
        .size:           8
        .value_kind:     global_buffer
      - .actual_access:  read_only
        .address_space:  global
        .offset:         24
        .size:           8
        .value_kind:     global_buffer
      - .actual_access:  read_only
        .address_space:  global
        .offset:         32
        .size:           8
        .value_kind:     global_buffer
      - .actual_access:  read_only
        .address_space:  global
        .offset:         40
        .size:           8
        .value_kind:     global_buffer
      - .actual_access:  read_only
        .address_space:  global
        .offset:         48
        .size:           8
        .value_kind:     global_buffer
      - .actual_access:  read_only
        .address_space:  global
        .offset:         56
        .size:           8
        .value_kind:     global_buffer
      - .actual_access:  read_only
        .address_space:  global
        .offset:         64
        .size:           8
        .value_kind:     global_buffer
      - .actual_access:  read_only
        .address_space:  global
        .offset:         72
        .size:           8
        .value_kind:     global_buffer
      - .actual_access:  read_only
        .address_space:  global
        .offset:         80
        .size:           8
        .value_kind:     global_buffer
      - .actual_access:  read_only
        .address_space:  global
        .offset:         88
        .size:           8
        .value_kind:     global_buffer
      - .actual_access:  read_only
        .address_space:  global
        .offset:         96
        .size:           8
        .value_kind:     global_buffer
      - .actual_access:  write_only
        .address_space:  global
        .offset:         104
        .size:           8
        .value_kind:     global_buffer
      - .actual_access:  write_only
        .address_space:  global
        .offset:         112
        .size:           8
        .value_kind:     global_buffer
      - .actual_access:  write_only
        .address_space:  global
        .offset:         120
        .size:           8
        .value_kind:     global_buffer
      - .actual_access:  write_only
        .address_space:  global
        .offset:         128
        .size:           8
        .value_kind:     global_buffer
      - .actual_access:  write_only
        .address_space:  global
        .offset:         136
        .size:           8
        .value_kind:     global_buffer
      - .actual_access:  write_only
        .address_space:  global
        .offset:         144
        .size:           8
        .value_kind:     global_buffer
      - .actual_access:  write_only
        .address_space:  global
        .offset:         152
        .size:           8
        .value_kind:     global_buffer
      - .actual_access:  write_only
        .address_space:  global
        .offset:         160
        .size:           8
        .value_kind:     global_buffer
      - .actual_access:  write_only
        .address_space:  global
        .offset:         168
        .size:           8
        .value_kind:     global_buffer
      - .actual_access:  read_only
        .address_space:  global
        .offset:         176
        .size:           8
        .value_kind:     global_buffer
    .group_segment_fixed_size: 29696
    .kernarg_segment_align: 8
    .kernarg_segment_size: 184
    .language:       OpenCL C
    .language_version:
      - 2
      - 0
    .max_flat_workgroup_size: 512
    .name:           _Z12front_kernelPKiS0_PKfS2_S2_S2_S2_S2_S2_S2_S2_S2_S2_PjS3_PiS4_PDF16_PfS6_S4_S5_S0_
    .private_segment_fixed_size: 0
    .sgpr_count:     30
    .sgpr_spill_count: 0
    .symbol:         _Z12front_kernelPKiS0_PKfS2_S2_S2_S2_S2_S2_S2_S2_S2_S2_PjS3_PiS4_PDF16_PfS6_S4_S5_S0_.kd
    .uniform_work_group_size: 1
    .uses_dynamic_stack: false
    .vgpr_count:     80
    .vgpr_spill_count: 0
    .wavefront_size: 64
  - .agpr_count:     0
    .args:
      - .actual_access:  read_only
        .address_space:  global
        .offset:         0
        .size:           8
        .value_kind:     global_buffer
      - .actual_access:  read_only
        .address_space:  global
        .offset:         8
        .size:           8
        .value_kind:     global_buffer
      - .actual_access:  write_only
        .address_space:  global
        .offset:         16
        .size:           8
        .value_kind:     global_buffer
      - .actual_access:  write_only
        .address_space:  global
        .offset:         24
        .size:           8
        .value_kind:     global_buffer
      - .actual_access:  write_only
        .address_space:  global
        .offset:         32
        .size:           8
        .value_kind:     global_buffer
      - .actual_access:  read_only
        .address_space:  global
        .offset:         40
        .size:           8
        .value_kind:     global_buffer
      - .actual_access:  read_only
        .address_space:  global
        .offset:         48
        .size:           8
        .value_kind:     global_buffer
      - .actual_access:  write_only
        .address_space:  global
        .offset:         56
        .size:           8
        .value_kind:     global_buffer
      - .actual_access:  write_only
        .address_space:  global
        .offset:         64
        .size:           8
        .value_kind:     global_buffer
    .group_segment_fixed_size: 40960
    .kernarg_segment_align: 8
    .kernarg_segment_size: 72
    .language:       OpenCL C
    .language_version:
      - 2
      - 0
    .max_flat_workgroup_size: 512
    .name:           _Z13second_kernelPKfPKDF16_PDF16_PfS4_PKjPKiPiS9_
    .private_segment_fixed_size: 0
    .sgpr_count:     34
    .sgpr_spill_count: 0
    .symbol:         _Z13second_kernelPKfPKDF16_PDF16_PfS4_PKjPKiPiS9_.kd
    .uniform_work_group_size: 1
    .uses_dynamic_stack: false
    .vgpr_count:     64
    .vgpr_spill_count: 0
    .wavefront_size: 64
  - .agpr_count:     0
    .args:
      - .actual_access:  read_only
        .address_space:  global
        .offset:         0
        .size:           8
        .value_kind:     global_buffer
      - .actual_access:  read_only
        .address_space:  global
        .offset:         8
        .size:           8
        .value_kind:     global_buffer
      - .actual_access:  read_only
        .address_space:  global
        .offset:         16
        .size:           8
        .value_kind:     global_buffer
      - .actual_access:  read_only
        .address_space:  global
        .offset:         24
        .size:           8
        .value_kind:     global_buffer
      - .actual_access:  read_only
        .address_space:  global
        .offset:         32
        .size:           8
        .value_kind:     global_buffer
      - .actual_access:  read_only
        .address_space:  global
        .offset:         40
        .size:           8
        .value_kind:     global_buffer
      - .actual_access:  read_only
        .address_space:  global
        .offset:         48
        .size:           8
        .value_kind:     global_buffer
      - .actual_access:  write_only
        .address_space:  global
        .offset:         56
        .size:           8
        .value_kind:     global_buffer
      - .actual_access:  write_only
        .address_space:  global
        .offset:         64
        .size:           8
        .value_kind:     global_buffer
      - .actual_access:  write_only
        .address_space:  global
        .offset:         72
        .size:           8
        .value_kind:     global_buffer
      - .offset:         80
        .size:           4
        .value_kind:     by_value
    .group_segment_fixed_size: 10256
    .kernarg_segment_align: 8
    .kernarg_segment_size: 84
    .language:       OpenCL C
    .language_version:
      - 2
      - 0
    .max_flat_workgroup_size: 256
    .name:           _Z11agg1_kernelPKDF16_PKfS2_PKiS4_S2_S2_PDF16_PfS6_i
    .private_segment_fixed_size: 0
    .sgpr_count:     54
    .sgpr_spill_count: 0
    .symbol:         _Z11agg1_kernelPKDF16_PKfS2_PKiS4_S2_S2_PDF16_PfS6_i.kd
    .uniform_work_group_size: 1
    .uses_dynamic_stack: false
    .vgpr_count:     70
    .vgpr_spill_count: 0
    .wavefront_size: 64
  - .agpr_count:     0
    .args:
      - .actual_access:  read_only
        .address_space:  global
        .offset:         0
        .size:           8
        .value_kind:     global_buffer
      - .actual_access:  read_only
        .address_space:  global
        .offset:         8
        .size:           8
        .value_kind:     global_buffer
      - .actual_access:  read_only
        .address_space:  global
        .offset:         16
        .size:           8
        .value_kind:     global_buffer
      - .actual_access:  read_only
        .address_space:  global
        .offset:         24
        .size:           8
        .value_kind:     global_buffer
      - .actual_access:  read_only
        .address_space:  global
        .offset:         32
        .size:           8
        .value_kind:     global_buffer
      - .actual_access:  write_only
        .address_space:  global
        .offset:         40
        .size:           8
        .value_kind:     global_buffer
      - .offset:         48
        .size:           4
        .value_kind:     by_value
    .group_segment_fixed_size: 0
    .kernarg_segment_align: 8
    .kernarg_segment_size: 52
    .language:       OpenCL C
    .language_version:
      - 2
      - 0
    .max_flat_workgroup_size: 256
    .name:           _Z13stats2_kernelPKiS0_PKfS2_S0_P15HIP_vector_typeIfLj4EEi
    .private_segment_fixed_size: 0
    .sgpr_count:     38
    .sgpr_spill_count: 0
    .symbol:         _Z13stats2_kernelPKiS0_PKfS2_S0_P15HIP_vector_typeIfLj4EEi.kd
    .uniform_work_group_size: 1
    .uses_dynamic_stack: false
    .vgpr_count:     32
    .vgpr_spill_count: 0
    .wavefront_size: 64
  - .agpr_count:     0
    .args:
      - .actual_access:  read_only
        .address_space:  global
        .offset:         0
        .size:           8
        .value_kind:     global_buffer
      - .actual_access:  read_only
        .address_space:  global
        .offset:         8
        .size:           8
        .value_kind:     global_buffer
      - .actual_access:  read_only
        .address_space:  global
        .offset:         16
        .size:           8
        .value_kind:     global_buffer
      - .actual_access:  read_only
        .address_space:  global
        .offset:         24
        .size:           8
        .value_kind:     global_buffer
      - .actual_access:  read_only
        .address_space:  global
        .offset:         32
        .size:           8
        .value_kind:     global_buffer
      - .actual_access:  write_only
        .address_space:  global
        .offset:         40
        .size:           8
        .value_kind:     global_buffer
      - .offset:         48
        .size:           4
        .value_kind:     by_value
    .group_segment_fixed_size: 70752
    .kernarg_segment_align: 8
    .kernarg_segment_size: 52
    .language:       OpenCL C
    .language_version:
      - 2
      - 0
    .max_flat_workgroup_size: 1024
    .name:           _Z12pool2_kernelPKjPKiPKfPK15HIP_vector_typeIfLj4EEPKDF16_Pfi
    .private_segment_fixed_size: 0
    .sgpr_count:     26
    .sgpr_spill_count: 0
    .symbol:         _Z12pool2_kernelPKjPKiPKfPK15HIP_vector_typeIfLj4EEPKDF16_Pfi.kd
    .uniform_work_group_size: 1
    .uses_dynamic_stack: false
    .vgpr_count:     128
    .vgpr_spill_count: 0
    .wavefront_size: 64
  - .agpr_count:     0
    .args:
      - .actual_access:  read_only
        .address_space:  global
        .offset:         0
        .size:           8
        .value_kind:     global_buffer
      - .actual_access:  read_only
        .address_space:  global
        .offset:         8
        .size:           8
        .value_kind:     global_buffer
      - .actual_access:  read_only
        .address_space:  global
        .offset:         16
        .size:           8
        .value_kind:     global_buffer
      - .actual_access:  read_only
        .address_space:  global
        .offset:         24
        .size:           8
        .value_kind:     global_buffer
      - .actual_access:  read_only
        .address_space:  global
        .offset:         32
        .size:           8
        .value_kind:     global_buffer
      - .actual_access:  read_only
        .address_space:  global
        .offset:         40
        .size:           8
        .value_kind:     global_buffer
      - .actual_access:  read_only
        .address_space:  global
        .offset:         48
        .size:           8
        .value_kind:     global_buffer
      - .actual_access:  read_only
        .address_space:  global
        .offset:         56
        .size:           8
        .value_kind:     global_buffer
      - .actual_access:  write_only
        .address_space:  global
        .offset:         64
        .size:           8
        .value_kind:     global_buffer
    .group_segment_fixed_size: 9472
    .kernarg_segment_align: 8
    .kernarg_segment_size: 72
    .language:       OpenCL C
    .language_version:
      - 2
      - 0
    .max_flat_workgroup_size: 1024
    .name:           _Z10mlp_kernelPKfPKiS0_S0_S0_S0_S0_S0_Pf
    .private_segment_fixed_size: 0
    .sgpr_count:     76
    .sgpr_spill_count: 0
    .symbol:         _Z10mlp_kernelPKfPKiS0_S0_S0_S0_S0_S0_Pf.kd
    .uniform_work_group_size: 1
    .uses_dynamic_stack: false
    .vgpr_count:     77
    .vgpr_spill_count: 0
    .wavefront_size: 64
